# early L2 write-back by the 28th of 32 arrivers per XCD on top of the flat barrier release
# speedup vs baseline: 1.0055x; 1.0001x over previous
; __device__ __forceinline__ unsigned xb_ld(unsigned* p)              { return __hip_atomic_load(p, __ATOMIC_RELAXED, __HIP_MEMORY_SCOPE_AGENT); }
; __device__ __forceinline__ unsigned xb_add(unsigned* p, unsigned v) { return __hip_atomic_fetch_add(p, v, __ATOMIC_RELAXED, __HIP_MEMORY_SCOPE_AGENT); }
; #define XB_SPIN(cond, bar) do { unsigned _sp = 0; while (cond) { __builtin_amdgcn_s_sleep(1); \
;     if ((++_sp & 255u) == 0u) { if (xb_ld(&(bar)[XB_TMO])) break; if (_sp > XB_SPIN_CAP) { atomicAdd(&(bar)[XB_TMO], 1u); break; } } } } while (0)
; __device__ __forceinline__ void xcd_barrier(const XcdBarrier& b, bool t0) {
;     ...
;         const unsigned old = xb_add(&bar[XB_XSUB(b.x)], 1u);
;         const unsigned gen = old / nloc;
;         if (old + 1u == (gen + 1u) * nloc) {
;             __builtin_amdgcn_fence(__ATOMIC_RELEASE, "agent");
;             asm volatile("s_waitcnt vmcnt(0)" ::: "memory");
;             const unsigned og = xb_add(&bar[XB_TOP], 1u);
;             const unsigned tg = og / nx;
;             if (og + 1u == (tg + 1u) * nx) xb_add(&bar[XB_TOPGEN], 1u);
;             else XB_SPIN(xb_ld(&bar[XB_TOPGEN]) == tg, bar);
;             __builtin_amdgcn_fence(__ATOMIC_ACQUIRE, "agent");
;             xb_add(&bar[XB_XGEN(b.x)], 1u);
;             asm volatile("s_waitcnt vmcnt(0)" ::: "memory");
;         } else {
;             XB_SPIN(xb_ld(&bar[XB_XGEN(b.x)]) == gen, bar);
.LBB0_214:
	v_readlane_b32 s3, v254, 45
	s_lshl_b32 s3, s3, 8
	v_readlane_b32 s6, v254, 43
	v_readlane_b32 s7, v254, 44
	s_add_u32 s6, s6, s3
	s_addc_u32 s7, s7, 0
	v_mov_b32_e32 v1, 0x1000
	v_mov_b32_e32 v3, 1
	v_sub_u32_e32 v4, 0, v2
	global_atomic_add v3, v1, v3, s[6:7] offset:1024 sc0
	v_cvt_f32_u32_e32 v1, v2
	v_rcp_iflag_f32_e32 v1, v1
	s_nop 0
	v_mul_f32_e32 v1, 0x4f7ffffe, v1
	v_cvt_u32_f32_e32 v1, v1
	v_mul_lo_u32 v4, v4, v1
	v_mul_hi_u32 v4, v1, v4
	v_add_u32_e32 v1, v1, v4
	s_waitcnt vmcnt(0)
	v_mul_hi_u32 v1, v3, v1
	v_mul_lo_u32 v4, v1, v2
	v_sub_u32_e32 v4, v3, v4
	v_add_u32_e32 v5, 1, v1
	v_cmp_ge_u32_e32 vcc, v4, v2
	v_add_u32_e32 v3, 1, v3
	s_nop 0
	v_cndmask_b32_e32 v1, v1, v5, vcc
	v_sub_u32_e32 v5, v4, v2
	v_cndmask_b32_e32 v4, v4, v5, vcc
	v_add_u32_e32 v5, 1, v1
	v_cmp_ge_u32_e32 vcc, v4, v2
	s_nop 1
	v_cndmask_b32_e32 v1, v1, v5, vcc
	v_mul_lo_u32 v4, v2, v1
	v_add_u32_e32 v2, v4, v2
	v_cmp_ne_u32_e32 vcc, v3, v2
	s_and_saveexec_b64 s[8:9], vcc
	s_xor_b64 s[8:9], exec, s[8:9]
	s_cbranch_execz .LBB0_228
	v_sub_u32_e32 v5, v2, v4
	v_sub_u32_e32 v3, v3, v4
	v_lshrrev_b32_e32 v4, 3, v5
	v_sub_u32_e32 v5, v5, v4
	v_cmp_ne_u32_e32 vcc, v3, v5
	s_cbranch_vccnz .Lef_skip_1
	buffer_wbl2 sc1
	s_waitcnt vmcnt(0)
.Lef_skip_1:
	s_waitcnt lgkmcnt(0)
	v_mov_b32_e32 v0, 0x7500
	global_load_dword v0, v0, s[46:47] sc1
	s_add_u32 s14, s46, 0x7500
	s_addc_u32 s15, s47, 0
	s_waitcnt vmcnt(0)
	v_cmp_eq_u32_e32 vcc, v0, v1
	s_and_saveexec_b64 s[10:11], vcc
	s_cbranch_execz .LBB0_227
	s_add_u32 s12, s46, 0x4200
	s_addc_u32 s13, s47, 0
	s_mov_b32 s3, 1
	s_mov_b64 s[16:17], 0
	v_mov_b32_e32 v0, 0
	s_branch .LBB0_218

; __device__ __forceinline__ unsigned xb_add(unsigned* p, unsigned v) { return __hip_atomic_fetch_add(p, v, __ATOMIC_RELAXED, __HIP_MEMORY_SCOPE_AGENT); }
; __device__ __forceinline__ void xcd_barrier(const XcdBarrier& b, bool t0) {
;     ...
;         const unsigned old = xb_add(&bar[XB_XSUB(b.x)], 1u);
;         const unsigned gen = old / nloc;
;         if (old + 1u == (gen + 1u) * nloc) {
.LBB0_479:
	v_readlane_b32 s3, v254, 45
	s_lshl_b32 s3, s3, 8
	v_readlane_b32 s6, v254, 43
	v_readlane_b32 s7, v254, 44
	s_add_u32 s6, s6, s3
	s_addc_u32 s7, s7, 0
	v_mov_b32_e32 v1, 0x1000
	v_mov_b32_e32 v4, 1
	v_sub_u32_e32 v5, 0, v3
	global_atomic_add v4, v1, v4, s[6:7] offset:1024 sc0
	v_cvt_f32_u32_e32 v1, v3
	v_rcp_iflag_f32_e32 v1, v1
	s_nop 0
	v_mul_f32_e32 v1, 0x4f7ffffe, v1
	v_cvt_u32_f32_e32 v1, v1
	v_mul_lo_u32 v5, v5, v1
	v_mul_hi_u32 v5, v1, v5
	v_add_u32_e32 v1, v1, v5
	s_waitcnt vmcnt(0)
	v_mul_hi_u32 v1, v4, v1
	v_mul_lo_u32 v5, v1, v3
	v_sub_u32_e32 v5, v4, v5
	v_add_u32_e32 v6, 1, v1
	v_cmp_ge_u32_e32 vcc, v5, v3
	v_add_u32_e32 v4, 1, v4
	s_nop 0
	v_cndmask_b32_e32 v1, v1, v6, vcc
	v_sub_u32_e32 v6, v5, v3
	v_cndmask_b32_e32 v5, v5, v6, vcc
	v_add_u32_e32 v6, 1, v1
	v_cmp_ge_u32_e32 vcc, v5, v3
	s_nop 1
	v_cndmask_b32_e32 v1, v1, v6, vcc
	v_mul_lo_u32 v5, v3, v1
	v_add_u32_e32 v3, v5, v3
	v_cmp_ne_u32_e32 vcc, v4, v3
	s_and_saveexec_b64 s[8:9], vcc
	s_xor_b64 s[8:9], exec, s[8:9]
	s_cbranch_execz .LBB0_493
	v_sub_u32_e32 v6, v3, v5
	v_sub_u32_e32 v4, v4, v5
	v_lshrrev_b32_e32 v5, 3, v6
	v_sub_u32_e32 v6, v6, v5
	v_cmp_ne_u32_e32 vcc, v4, v6
	s_cbranch_vccnz .Lef_skip_3
	buffer_wbl2 sc1
	s_waitcnt vmcnt(0)

; __device__ __forceinline__ unsigned xb_add(unsigned* p, unsigned v) { return __hip_atomic_fetch_add(p, v, __ATOMIC_RELAXED, __HIP_MEMORY_SCOPE_AGENT); }
; __device__ __forceinline__ void xcd_barrier(const XcdBarrier& b, bool t0) {
;     ...
;         const unsigned old = xb_add(&bar[XB_XSUB(b.x)], 1u);
;         const unsigned gen = old / nloc;
;         if (old + 1u == (gen + 1u) * nloc) {
.LBB0_534:
	v_readlane_b32 s3, v254, 45
	s_lshl_b32 s3, s3, 8
	v_readlane_b32 s6, v254, 43
	v_readlane_b32 s7, v254, 44
	s_add_u32 s6, s6, s3
	s_addc_u32 s7, s7, 0
	v_mov_b32_e32 v1, 0x1000
	v_mov_b32_e32 v5, 1
	v_sub_u32_e32 v6, 0, v4
	global_atomic_add v5, v1, v5, s[6:7] offset:1024 sc0
	v_cvt_f32_u32_e32 v1, v4
	v_rcp_iflag_f32_e32 v1, v1
	s_nop 0
	v_mul_f32_e32 v1, 0x4f7ffffe, v1
	v_cvt_u32_f32_e32 v1, v1
	v_mul_lo_u32 v6, v6, v1
	v_mul_hi_u32 v6, v1, v6
	v_add_u32_e32 v1, v1, v6
	s_waitcnt vmcnt(0)
	v_mul_hi_u32 v1, v5, v1
	v_mul_lo_u32 v6, v1, v4
	v_sub_u32_e32 v6, v5, v6
	v_add_u32_e32 v7, 1, v1
	v_cmp_ge_u32_e32 vcc, v6, v4
	v_add_u32_e32 v5, 1, v5
	s_nop 0
	v_cndmask_b32_e32 v1, v1, v7, vcc
	v_sub_u32_e32 v7, v6, v4
	v_cndmask_b32_e32 v6, v6, v7, vcc
	v_add_u32_e32 v7, 1, v1
	v_cmp_ge_u32_e32 vcc, v6, v4
	s_nop 1
	v_cndmask_b32_e32 v1, v1, v7, vcc
	v_mul_lo_u32 v6, v4, v1
	v_add_u32_e32 v4, v6, v4
	v_cmp_ne_u32_e32 vcc, v5, v4
	s_and_saveexec_b64 s[8:9], vcc
	s_xor_b64 s[8:9], exec, s[8:9]
	s_cbranch_execz .LBB0_548
	v_sub_u32_e32 v7, v4, v6
	v_sub_u32_e32 v5, v5, v6
	v_lshrrev_b32_e32 v6, 3, v7
	v_sub_u32_e32 v7, v7, v6
	v_cmp_ne_u32_e32 vcc, v5, v7
	s_cbranch_vccnz .Lef_skip_4
	buffer_wbl2 sc1
	s_waitcnt vmcnt(0)

; __device__ __forceinline__ unsigned xb_ld(unsigned* p)              { return __hip_atomic_load(p, __ATOMIC_RELAXED, __HIP_MEMORY_SCOPE_AGENT); }
; __device__ __forceinline__ unsigned xb_add(unsigned* p, unsigned v) { return __hip_atomic_fetch_add(p, v, __ATOMIC_RELAXED, __HIP_MEMORY_SCOPE_AGENT); }
; #define XB_SPIN(cond, bar) do { unsigned _sp = 0; while (cond) { __builtin_amdgcn_s_sleep(1); \
;     if ((++_sp & 255u) == 0u) { if (xb_ld(&(bar)[XB_TMO])) break; if (_sp > XB_SPIN_CAP) { atomicAdd(&(bar)[XB_TMO], 1u); break; } } } } while (0)
; __device__ __forceinline__ void xcd_barrier(const XcdBarrier& b, bool t0) {
;     ...
;         const unsigned old = xb_add(&bar[XB_XSUB(b.x)], 1u);
;         const unsigned gen = old / nloc;
;         if (old + 1u == (gen + 1u) * nloc) {
;             __builtin_amdgcn_fence(__ATOMIC_RELEASE, "agent");
;             asm volatile("s_waitcnt vmcnt(0)" ::: "memory");
;             const unsigned og = xb_add(&bar[XB_TOP], 1u);
;             const unsigned tg = og / nx;
;             if (og + 1u == (tg + 1u) * nx) xb_add(&bar[XB_TOPGEN], 1u);
;             else XB_SPIN(xb_ld(&bar[XB_TOPGEN]) == tg, bar);
;             __builtin_amdgcn_fence(__ATOMIC_ACQUIRE, "agent");
;             xb_add(&bar[XB_XGEN(b.x)], 1u);
;             asm volatile("s_waitcnt vmcnt(0)" ::: "memory");
;         } else {
;             XB_SPIN(xb_ld(&bar[XB_XGEN(b.x)]) == gen, bar);
.LBB0_1646:
	v_readlane_b32 s3, v254, 45
	s_lshl_b32 s3, s3, 8
	v_readlane_b32 s4, v254, 43
	v_readlane_b32 s5, v254, 44
	s_add_u32 s4, s4, s3
	s_addc_u32 s5, s5, 0
	v_mov_b32_e32 v1, 0x1000
	v_mov_b32_e32 v3, 1
	v_sub_u32_e32 v4, 0, v2
	global_atomic_add v3, v1, v3, s[4:5] offset:1024 sc0
	v_cvt_f32_u32_e32 v1, v2
	v_rcp_iflag_f32_e32 v1, v1
	s_nop 0
	v_mul_f32_e32 v1, 0x4f7ffffe, v1
	v_cvt_u32_f32_e32 v1, v1
	v_mul_lo_u32 v4, v4, v1
	v_mul_hi_u32 v4, v1, v4
	v_add_u32_e32 v1, v1, v4
	s_waitcnt vmcnt(0)
	v_mul_hi_u32 v1, v3, v1
	v_mul_lo_u32 v4, v1, v2
	v_sub_u32_e32 v4, v3, v4
	v_add_u32_e32 v5, 1, v1
	v_cmp_ge_u32_e32 vcc, v4, v2
	v_add_u32_e32 v3, 1, v3
	s_nop 0
	v_cndmask_b32_e32 v1, v1, v5, vcc
	v_sub_u32_e32 v5, v4, v2
	v_cndmask_b32_e32 v4, v4, v5, vcc
	v_add_u32_e32 v5, 1, v1
	v_cmp_ge_u32_e32 vcc, v4, v2
	s_nop 1
	v_cndmask_b32_e32 v1, v1, v5, vcc
	v_mul_lo_u32 v4, v2, v1
	v_add_u32_e32 v2, v4, v2
	v_cmp_ne_u32_e32 vcc, v3, v2
	s_and_saveexec_b64 s[6:7], vcc
	s_xor_b64 s[6:7], exec, s[6:7]
	s_cbranch_execz .LBB0_1660
	v_sub_u32_e32 v5, v2, v4
	v_sub_u32_e32 v3, v3, v4
	v_lshrrev_b32_e32 v4, 3, v5
	v_sub_u32_e32 v5, v5, v4
	v_cmp_ne_u32_e32 vcc, v3, v5
	s_cbranch_vccnz .Lef_skip_11
	buffer_wbl2 sc1
	s_waitcnt vmcnt(0)
.Lef_skip_11:
	s_waitcnt lgkmcnt(0)
	v_mov_b32_e32 v0, 0x7500
	global_load_dword v0, v0, s[46:47] sc1
	s_add_u32 s12, s46, 0x7500
	s_addc_u32 s13, s47, 0
	s_waitcnt vmcnt(0)
	v_cmp_eq_u32_e32 vcc, v0, v1
	s_and_saveexec_b64 s[8:9], vcc
	s_cbranch_execz .LBB0_1659
	s_add_u32 s10, s46, 0x4200
	s_addc_u32 s11, s47, 0
	s_mov_b32 s3, 1
	s_mov_b64 s[14:15], 0
	v_mov_b32_e32 v0, 0
	s_branch .LBB0_1650
